# conversion streams + drains: next item's 16 loads issued before waiting for the current item's (two batches in flight per wave); top-of-half waits relaxed, vmcnt(20) after the loads in the P1 stream
# baseline (speedup 1.0000x reference)
; #define LAS __attribute__((address_space(3)))
; __device__ __forceinline__ unsigned stop_poll(const Ctx& c, const unsigned* p) {
;     volatile LAS unsigned* w = (volatile LAS unsigned*)(c.lds + STOPW_OFF);
;     if (c.wave == 0) { const unsigned v = __hip_atomic_load(p, __ATOMIC_RELAXED, __HIP_MEMORY_SCOPE_AGENT); if (c.lane == 0) *w = v; return (unsigned)__builtin_amdgcn_readfirstlane((int)v); }
;     return *w;
; __device__ __forceinline__ int conv_stream(const Ctx& c, int j, int first, int step, const unsigned* stop, const float* w_gu, const float* w_d, unsigned char* Wgu, unsigned char* Wd) {
;     ...
;         { const int i2 = i + step; const bool more = j + CONV_SLOTS * i2 < CONV_TOTAL && !(stop && stop_poll(c, stop) >= STOP_AT);
;           cs_load(j + CONV_SLOTS * (more ? i2 : i), c.lane, w_gu, w_d, vb);
;           cs_store(c, j + CONV_SLOTS * i, va, Wgu, Wd); i = i2; if (!more) break; }
.LBB0_259:
	s_add_i32 s24, s19, 0xfffffc00
	s_cmp_gt_i32 s24, 0x17fff
	s_mov_b64 s[44:45], 0
	s_cbranch_scc1 .LBB0_267
	s_mov_b64 s[44:45], -1
	s_and_b64 vcc, exec, s[6:7]
	s_cbranch_vccz .LBB0_262
	s_nop 0
	v_mov_b32_e32 v66, s18
	ds_read_b32 v66, v66
	s_mov_b64 s[44:45], 0
	s_waitcnt lgkmcnt(0)
	v_readfirstlane_b32 s20, v66

; __device__ __forceinline__ void t128_load(const float* W, int N, int item, int lane, f32x4 (&v)[16]) {
;     const int nblk = N / 32, kb = item / nblk, nb = item % nblk, k0 = 128 * kb, n0 = 32 * nb;
; #pragma unroll
;     for (int i = 0; i < 16; ++i) v[i] = __builtin_nontemporal_load((const f32x4*)(W + (size_t)(k0 + i * 8 + (lane >> 3)) * N + n0 + (lane & 7) * 4));
; __device__ __forceinline__ int conv_stream(const Ctx& c, int j, int first, int step, const unsigned* stop, const float* w_gu, const float* w_d, unsigned char* Wgu, unsigned char* Wd) {
;     ...
;         { const int i2 = i + step; const bool more = j + CONV_SLOTS * i2 < CONV_TOTAL && !(stop && stop_poll(c, stop) >= STOP_AT);
;           cs_load(j + CONV_SLOTS * (more ? i2 : i), c.lane, w_gu, w_d, vb);
;           cs_store(c, j + CONV_SLOTS * i, va, Wgu, Wd); i = i2; if (!more) break; }
.LBB0_271:
	s_nop 0
	v_or_b32_e32 v122, s21, v131
	v_ashrrev_i32_e32 v123, 31, v122
	v_lshlrev_b64 v[66:67], s46, v[122:123]
	v_add_u32_e32 v68, 8, v122
	v_add_u32_e32 v74, 16, v122
	v_add_u32_e32 v76, 24, v122
	v_add_u32_e32 v82, 32, v122
	v_add_u32_e32 v84, 40, v122
	v_add_u32_e32 v90, 48, v122
	v_add_u32_e32 v92, 56, v122
	v_add_u32_e32 v98, 64, v122
	v_add_u32_e32 v100, 0x48, v122
	v_add_u32_e32 v106, 0x50, v122
	v_add_u32_e32 v108, 0x58, v122
	v_add_u32_e32 v114, 0x60, v122
	v_add_u32_e32 v116, 0x68, v122
	v_add_u32_e32 v126, 0x70, v122
	v_add_u32_e32 v122, 0x78, v122
	v_lshlrev_b32_e32 v132, 2, v130
	v_ashrrev_i32_e32 v69, 31, v68
	v_ashrrev_i32_e32 v75, 31, v74
	v_ashrrev_i32_e32 v77, 31, v76
	v_ashrrev_i32_e32 v83, 31, v82
	v_ashrrev_i32_e32 v85, 31, v84
	v_ashrrev_i32_e32 v91, 31, v90
	v_ashrrev_i32_e32 v93, 31, v92
	v_ashrrev_i32_e32 v99, 31, v98
	v_ashrrev_i32_e32 v101, 31, v100
	v_ashrrev_i32_e32 v107, 31, v106
	v_ashrrev_i32_e32 v109, 31, v108
	v_ashrrev_i32_e32 v115, 31, v114
	v_ashrrev_i32_e32 v117, 31, v116
	v_ashrrev_i32_e32 v127, 31, v126
	v_ashrrev_i32_e32 v123, 31, v122
	v_lshl_add_u64 v[124:125], s[48:49], 0, v[132:133]
	v_lshlrev_b64 v[68:69], s46, v[68:69]
	v_lshlrev_b64 v[74:75], s46, v[74:75]
	v_lshlrev_b64 v[76:77], s46, v[76:77]
	v_lshlrev_b64 v[82:83], s46, v[82:83]
	v_lshlrev_b64 v[84:85], s46, v[84:85]
	v_lshlrev_b64 v[90:91], s46, v[90:91]
	v_lshlrev_b64 v[92:93], s46, v[92:93]
	v_lshlrev_b64 v[98:99], s46, v[98:99]
	v_lshlrev_b64 v[100:101], s46, v[100:101]
	v_lshlrev_b64 v[106:107], s46, v[106:107]
	v_lshlrev_b64 v[108:109], s46, v[108:109]
	v_lshlrev_b64 v[114:115], s46, v[114:115]
	v_lshlrev_b64 v[116:117], s46, v[116:117]
	v_lshlrev_b64 v[126:127], s46, v[126:127]
	v_lshlrev_b64 v[122:123], s46, v[122:123]
	v_lshl_add_u64 v[66:67], v[124:125], 0, v[66:67]
	v_lshl_add_u64 v[68:69], v[124:125], 0, v[68:69]
	v_lshl_add_u64 v[74:75], v[124:125], 0, v[74:75]
	v_lshl_add_u64 v[76:77], v[124:125], 0, v[76:77]
	v_lshl_add_u64 v[82:83], v[124:125], 0, v[82:83]
	v_lshl_add_u64 v[84:85], v[124:125], 0, v[84:85]
	v_lshl_add_u64 v[90:91], v[124:125], 0, v[90:91]
	v_lshl_add_u64 v[92:93], v[124:125], 0, v[92:93]
	v_lshl_add_u64 v[98:99], v[124:125], 0, v[98:99]
	v_lshl_add_u64 v[100:101], v[124:125], 0, v[100:101]
	v_lshl_add_u64 v[106:107], v[124:125], 0, v[106:107]
	v_lshl_add_u64 v[108:109], v[124:125], 0, v[108:109]
	v_lshl_add_u64 v[114:115], v[124:125], 0, v[114:115]
	v_lshl_add_u64 v[116:117], v[124:125], 0, v[116:117]
	v_lshl_add_u64 v[126:127], v[124:125], 0, v[126:127]
	v_lshl_add_u64 v[122:123], v[124:125], 0, v[122:123]
	s_and_b64 vcc, exec, s[44:45]
	s_cbranch_vccz .LLcv1a_noload_w
	global_load_dwordx4 v[70:73], v[66:67], off nt
	s_nop 0
	global_load_dwordx4 v[66:69], v[68:69], off nt
	s_nop 0
	global_load_dwordx4 v[78:81], v[74:75], off nt
	s_nop 0
	global_load_dwordx4 v[74:77], v[76:77], off nt
	s_nop 0
	global_load_dwordx4 v[86:89], v[82:83], off nt
	s_nop 0
	global_load_dwordx4 v[82:85], v[84:85], off nt
	s_nop 0
	global_load_dwordx4 v[94:97], v[90:91], off nt
	s_nop 0
	global_load_dwordx4 v[90:93], v[92:93], off nt
	s_nop 0
	global_load_dwordx4 v[102:105], v[98:99], off nt
	s_nop 0
	global_load_dwordx4 v[98:101], v[100:101], off nt
	s_nop 0
	global_load_dwordx4 v[110:113], v[106:107], off nt
	s_nop 0
	global_load_dwordx4 v[106:109], v[108:109], off nt
	s_nop 0
	global_load_dwordx4 v[118:121], v[114:115], off nt
	s_nop 0
	global_load_dwordx4 v[114:117], v[116:117], off nt
	s_nop 0
	global_load_dwordx4 v[126:129], v[126:127], off nt
	s_nop 0
	global_load_dwordx4 v[122:125], v[122:123], off nt
	s_waitcnt vmcnt(20)
	s_branch .Lcv1a_noload
.LLcv1a_noload_w:
	s_waitcnt vmcnt(4)
.Lcv1a_noload:
	s_add_i32 s26, s19, 0xfffff800
	s_mov_b64 s[46:47], -1
	s_cmpk_gt_i32 s26, 0x7fff
	v_add_u32_e32 v156, 0x1080, v146
	v_add_u32_e32 v157, 0x1088, v146
	v_add_u32_e32 v158, 0x14a0, v146
	v_add_u32_e32 v159, 0x14a8, v146
	v_add_u32_e32 v160, 0x18c0, v146
	v_add_u32_e32 v161, 0x18c8, v146
	v_add_u32_e32 v162, 0x1ce0, v146
	v_add_u32_e32 v163, 0x1ce8, v146
	v_add_u32_e32 v164, 0x2100, v146
	v_add_u32_e32 v165, 0x2108, v146
	v_add_u32_e32 v166, 0x2520, v146
	v_add_u32_e32 v167, 0x2528, v146
	v_add_u32_e32 v168, 0x2940, v146
	v_add_u32_e32 v169, 0x2948, v146
	v_add_u32_e32 v170, 0x2d60, v146
	v_add_u32_e32 v171, 0x2d68, v146
	v_add_u32_e32 v172, 0x3180, v146
	v_add_u32_e32 v173, 0x3188, v146
	v_add_u32_e32 v174, 0x35a0, v146
	v_add_u32_e32 v175, 0x35a8, v146
	v_add_u32_e32 v176, 0x39c0, v146
	v_add_u32_e32 v177, 0x39c8, v146
	v_add_u32_e32 v178, 0x3de0, v146
	v_add_u32_e32 v179, 0x3de8, v146
	v_add_u32_e32 v155, 0x400, v150
	v_add_u32_e32 v154, 0x600, v150
	s_cbranch_scc0 .LBB0_290
; #define LAS __attribute__((address_space(3)))
; #define LDS_WAIT() asm volatile("s_waitcnt lgkmcnt(0)" ::: "memory")
; template <int MODE>
; __device__ __forceinline__ void t128_store(const Ctx& c, const f32x4 (&v)[16], int K, int N, unsigned char* WT, int item) {
;     LAS float* scr = (LAS float*)(c.lds + c.wave * CONV_SCR);
;     const int nblk = N / 32, kb = item / nblk, nb = item % nblk, k0 = 128 * kb, n0 = 32 * nb, lane = c.lane;
; #pragma unroll
;     for (int i = 0; i < 16; ++i) { LAS float* d = scr + (i * 8 + (lane >> 3)) * 33 + (lane & 7) * 4; d[0] = v[i].x; d[1] = v[i].y; d[2] = v[i].z; d[3] = v[i].w; }
;     LDS_WAIT(); asm volatile("" ::: "memory");
;     const int cc = lane & 7;
; #pragma unroll
;     for (int j = 0; j < 4; ++j) { const int n = (lane >> 3) + 8 * j; const LAS float* s = scr + (16 * cc) * 33 + n; int w[4];
; #pragma unroll
;         for (int q = 0; q < 4; ++q) { int t = 0; t = __builtin_amdgcn_cvt_pk_fp8_f32(s[(4 * q) * 33] * WSCALE, s[(4 * q + 1) * 33] * WSCALE, t, false);
;             t = __builtin_amdgcn_cvt_pk_fp8_f32(s[(4 * q + 2) * 33] * WSCALE, s[(4 * q + 3) * 33] * WSCALE, t, true); w[q] = t; }
	s_nop 0
	ds_write2_b32 v146, v6, v7 offset1:1
	ds_write2_b32 v146, v8, v9 offset0:2 offset1:3
	ds_write2_b32 v151, v2, v3 offset1:1
	ds_write2_b32 v151, v4, v5 offset0:2 offset1:3
	ds_write2_b32 v152, v14, v15 offset1:1
	ds_write2_b32 v152, v16, v17 offset0:2 offset1:3
	ds_write2_b32 v153, v10, v11 offset1:1
	ds_write2_b32 v153, v12, v13 offset0:2 offset1:3
	ds_write2_b32 v156, v22, v23 offset1:1
	ds_write2_b32 v157, v24, v25 offset1:1
	ds_write2_b32 v158, v18, v19 offset1:1
	ds_write2_b32 v159, v20, v21 offset1:1
	ds_write2_b32 v160, v30, v31 offset1:1
	ds_write2_b32 v161, v32, v33 offset1:1
	ds_write2_b32 v162, v26, v27 offset1:1
	ds_write2_b32 v163, v28, v29 offset1:1
	ds_write2_b32 v164, v38, v39 offset1:1
	ds_write2_b32 v165, v40, v41 offset1:1
	ds_write2_b32 v166, v34, v35 offset1:1
	ds_write2_b32 v167, v36, v37 offset1:1
	ds_write2_b32 v168, v46, v47 offset1:1
	ds_write2_b32 v169, v48, v49 offset1:1
	ds_write2_b32 v170, v42, v43 offset1:1
	ds_write2_b32 v171, v44, v45 offset1:1
	ds_write2_b32 v172, v54, v55 offset1:1
	ds_write2_b32 v173, v56, v57 offset1:1
	ds_write2_b32 v174, v50, v51 offset1:1
	ds_write2_b32 v175, v52, v53 offset1:1
	ds_write2_b32 v176, v62, v63 offset1:1
	ds_write2_b32 v177, v64, v65 offset1:1
	ds_write2_b32 v178, v58, v59 offset1:1
	ds_write2_b32 v179, v60, v61 offset1:1
	s_waitcnt lgkmcnt(0)
	ds_read2_b32 v[184:185], v150 offset1:8
	ds_read2_b32 v[186:187], v150 offset0:33 offset1:41
	ds_read2_b32 v[190:191], v150 offset0:66 offset1:74
	ds_read2_b32 v[192:193], v150 offset0:99 offset1:107
	v_mov_b32_e32 v180, v133
	ds_read2_b32 v[194:195], v150 offset0:132 offset1:140
	ds_read2_b32 v[196:197], v150 offset0:165 offset1:173
	s_waitcnt lgkmcnt(5)
	v_mul_f32_e32 v181, 0x42800000, v184
	s_waitcnt lgkmcnt(4)
	v_mul_f32_e32 v182, 0x42800000, v186
	v_cvt_pk_fp8_f32 v180, v181, v182
	s_waitcnt lgkmcnt(3)
	v_mul_f32_e32 v181, 0x42800000, v190
	s_waitcnt lgkmcnt(2)
	v_mul_f32_e32 v182, 0x42800000, v192
	ds_read2_b32 v[198:199], v150 offset0:198 offset1:206
	ds_read2_b32 v[200:201], v150 offset0:231 offset1:239
	v_cvt_pk_fp8_f32 v180, v181, v182 op_sel:[0,0,1]
	s_waitcnt lgkmcnt(3)
	v_mul_f32_e32 v182, 0x42800000, v194
	s_waitcnt lgkmcnt(2)
	v_mul_f32_e32 v183, 0x42800000, v196
	v_mov_b32_e32 v181, v133
	ds_read2_b32 v[202:203], v155 offset0:8 offset1:16
	ds_read2_b32 v[204:205], v155 offset0:41 offset1:49
	v_cvt_pk_fp8_f32 v181, v182, v183
	ds_read2_b32 v[206:207], v155 offset0:74 offset1:82
	ds_read2_b32 v[208:209], v155 offset0:107 offset1:115
	ds_read2_b32 v[210:211], v155 offset0:140 offset1:148
	ds_read2_b32 v[212:213], v155 offset0:173 offset1:181
	s_waitcnt lgkmcnt(7)
	v_mul_f32_e32 v182, 0x42800000, v198
	s_waitcnt lgkmcnt(6)
	v_mul_f32_e32 v183, 0x42800000, v200
	v_cvt_pk_fp8_f32 v181, v182, v183 op_sel:[0,0,1]
	s_waitcnt lgkmcnt(5)
	v_mul_f32_e32 v183, 0x42800000, v202
	s_waitcnt lgkmcnt(4)
	v_mul_f32_e32 v184, 0x42800000, v204
	v_mov_b32_e32 v182, v133
	ds_read2_b32 v[214:215], v155 offset0:206 offset1:214
	ds_read2_b32 v[216:217], v155 offset0:239 offset1:247
	v_cvt_pk_fp8_f32 v182, v183, v184
	s_waitcnt lgkmcnt(3)
	v_mul_f32_e32 v190, 0x42800000, v210
	s_waitcnt lgkmcnt(2)
	v_mul_f32_e32 v192, 0x42800000, v212
	v_mov_b32_e32 v183, v133
	v_cvt_pk_fp8_f32 v183, v190, v192
	v_mul_f32_e32 v184, 0x42800000, v206
	v_mul_f32_e32 v186, 0x42800000, v208
	v_cvt_pk_fp8_f32 v182, v184, v186 op_sel:[0,0,1]
	s_waitcnt lgkmcnt(1)
	v_mul_f32_e32 v184, 0x42800000, v214
	s_waitcnt lgkmcnt(0)
; #define LAS __attribute__((address_space(3)))
; template <int MODE>
; __device__ __forceinline__ void t128_store(const Ctx& c, const f32x4 (&v)[16], int K, int N, unsigned char* WT, int item) {
;     ...
;     for (int j = 0; j < 4; ++j) { const int n = (lane >> 3) + 8 * j; const LAS float* s = scr + (16 * cc) * 33 + n; int w[4];
; #pragma unroll
;         for (int q = 0; q < 4; ++q) { int t = 0; t = __builtin_amdgcn_cvt_pk_fp8_f32(s[(4 * q) * 33] * WSCALE, s[(4 * q + 1) * 33] * WSCALE, t, false);
;             t = __builtin_amdgcn_cvt_pk_fp8_f32(s[(4 * q + 2) * 33] * WSCALE, s[(4 * q + 3) * 33] * WSCALE, t, true); w[q] = t; }
;         const int dr = drow_of<MODE>(n0 + n);
;         __builtin_nontemporal_store((u32x4){(unsigned)w[0], (unsigned)w[1], (unsigned)w[2], (unsigned)w[3]}, (u32x4*)(WT + (size_t)dr * K + k0 + 16 * cc)); }
	v_mul_f32_e32 v186, 0x42800000, v216
	v_cvt_pk_fp8_f32 v183, v184, v186 op_sel:[0,0,1]
	v_mul_f32_e32 v185, 0x42800000, v185
	v_mul_f32_e32 v186, 0x42800000, v187
	v_mov_b32_e32 v184, v133
	v_cvt_pk_fp8_f32 v184, v185, v186
	v_mul_f32_e32 v186, 0x42800000, v191
	v_mul_f32_e32 v190, 0x42800000, v195
	v_mul_f32_e32 v191, 0x42800000, v197
	v_mov_b32_e32 v185, v133
	v_cvt_pk_fp8_f32 v185, v190, v191
	v_mul_f32_e32 v187, 0x42800000, v193
	v_cvt_pk_fp8_f32 v184, v186, v187 op_sel:[0,0,1]
	v_mul_f32_e32 v186, 0x42800000, v199
	v_mul_f32_e32 v187, 0x42800000, v201
	v_cvt_pk_fp8_f32 v185, v186, v187 op_sel:[0,0,1]
	v_mul_f32_e32 v187, 0x42800000, v203
	v_mul_f32_e32 v190, 0x42800000, v205
	v_mov_b32_e32 v186, v133
	v_cvt_pk_fp8_f32 v186, v187, v190
	v_mul_f32_e32 v192, 0x42800000, v211
	v_mul_f32_e32 v193, 0x42800000, v213
	v_mov_b32_e32 v187, v133
	v_cvt_pk_fp8_f32 v187, v192, v193
	s_add_i32 s20, s19, 0xffff7800
	v_mul_f32_e32 v190, 0x42800000, v207
	v_mul_f32_e32 v191, 0x42800000, v209
	s_lshr_b32 s42, s20, 11
	v_cvt_pk_fp8_f32 v186, v190, v191 op_sel:[0,0,1]
	v_mul_f32_e32 v190, 0x42800000, v215
	v_mul_f32_e32 v191, 0x42800000, v217
	s_lshl_b64 s[20:21], s[42:43], 23
	v_cvt_pk_fp8_f32 v187, v190, v191 op_sel:[0,0,1]
	v_lshl_add_u64 v[188:189], v[136:137], 0, s[20:21]
	ds_read2_b32 v[190:191], v150 offset0:16 offset1:24
	ds_read2_b32 v[192:193], v150 offset0:49 offset1:57
	v_lshl_add_u64 v[218:219], v[188:189], 0, v[138:139]
	global_store_dwordx4 v[218:219], v[180:183], off nt
	s_nop 1
	v_lshl_add_u64 v[180:181], v[188:189], 0, v[140:141]
	global_store_dwordx4 v[180:181], v[184:187], off nt
	ds_read2_b32 v[184:185], v150 offset0:82 offset1:90
	ds_read2_b32 v[186:187], v150 offset0:115 offset1:123
	s_waitcnt lgkmcnt(3)
	v_mul_f32_e32 v181, 0x42800000, v190
	s_waitcnt lgkmcnt(2)
	v_mul_f32_e32 v182, 0x42800000, v192
	v_mov_b32_e32 v180, v133
	ds_read2_b32 v[194:195], v150 offset0:148 offset1:156
	ds_read2_b32 v[196:197], v150 offset0:181 offset1:189
	v_cvt_pk_fp8_f32 v180, v181, v182
	s_waitcnt lgkmcnt(3)
	v_mul_f32_e32 v181, 0x42800000, v184
	s_waitcnt lgkmcnt(2)
	v_mul_f32_e32 v182, 0x42800000, v186
	ds_read2_b32 v[198:199], v150 offset0:214 offset1:222
	ds_read2_b32 v[200:201], v150 offset0:247 offset1:255
	v_cvt_pk_fp8_f32 v180, v181, v182 op_sel:[0,0,1]
	s_waitcnt lgkmcnt(3)
	v_mul_f32_e32 v182, 0x42800000, v194
	s_waitcnt lgkmcnt(2)
	v_mul_f32_e32 v183, 0x42800000, v196
	v_mov_b32_e32 v181, v133
	ds_read2_b32 v[202:203], v155 offset0:24 offset1:32
	ds_read2_b32 v[204:205], v155 offset0:57 offset1:65
	v_cvt_pk_fp8_f32 v181, v182, v183
	ds_read2_b32 v[206:207], v155 offset0:90 offset1:98
	ds_read2_b32 v[208:209], v155 offset0:123 offset1:131
	ds_read2_b32 v[210:211], v155 offset0:156 offset1:164
	ds_read2_b32 v[212:213], v155 offset0:189 offset1:197
	s_waitcnt lgkmcnt(7)
	v_mul_f32_e32 v182, 0x42800000, v198
	s_waitcnt lgkmcnt(6)
	v_mul_f32_e32 v183, 0x42800000, v200
	v_cvt_pk_fp8_f32 v181, v182, v183 op_sel:[0,0,1]
	s_waitcnt lgkmcnt(5)
	v_mul_f32_e32 v183, 0x42800000, v202
	s_waitcnt lgkmcnt(4)
	v_mul_f32_e32 v184, 0x42800000, v204
	v_mov_b32_e32 v182, v133
	ds_read2_b32 v[214:215], v155 offset0:222 offset1:230
	ds_read2_b32 v[216:217], v154 offset0:127 offset1:135
	v_cvt_pk_fp8_f32 v182, v183, v184
	s_waitcnt lgkmcnt(3)
	v_mul_f32_e32 v190, 0x42800000, v210
	s_waitcnt lgkmcnt(2)
	v_mul_f32_e32 v192, 0x42800000, v212
	v_mov_b32_e32 v183, v133
	v_cvt_pk_fp8_f32 v183, v190, v192
	v_mul_f32_e32 v184, 0x42800000, v206
	v_mul_f32_e32 v186, 0x42800000, v208
	v_cvt_pk_fp8_f32 v182, v184, v186 op_sel:[0,0,1]
	s_waitcnt lgkmcnt(1)
	v_mul_f32_e32 v184, 0x42800000, v214
	s_waitcnt lgkmcnt(0)
	v_mul_f32_e32 v186, 0x42800000, v216
	v_cvt_pk_fp8_f32 v183, v184, v186 op_sel:[0,0,1]
	v_mul_f32_e32 v186, 0x42800000, v191
	v_mul_f32_e32 v190, 0x42800000, v193
	v_mov_b32_e32 v184, v133
	v_cvt_pk_fp8_f32 v184, v186, v190
	v_mul_f32_e32 v186, 0x42800000, v185
	v_mul_f32_e32 v190, 0x42800000, v195
	v_mul_f32_e32 v191, 0x42800000, v197
	v_mov_b32_e32 v185, v133
	v_cvt_pk_fp8_f32 v185, v190, v191
	v_mul_f32_e32 v187, 0x42800000, v187
	v_cvt_pk_fp8_f32 v184, v186, v187 op_sel:[0,0,1]
	v_mul_f32_e32 v186, 0x42800000, v199
	v_mul_f32_e32 v187, 0x42800000, v201
	v_cvt_pk_fp8_f32 v185, v186, v187 op_sel:[0,0,1]
	v_mul_f32_e32 v187, 0x42800000, v203
	v_mul_f32_e32 v190, 0x42800000, v205
	v_mov_b32_e32 v186, v133
	v_cvt_pk_fp8_f32 v186, v187, v190
	v_mul_f32_e32 v192, 0x42800000, v211
	v_mul_f32_e32 v193, 0x42800000, v213
	v_mov_b32_e32 v187, v133
	v_cvt_pk_fp8_f32 v187, v192, v193
	v_mul_f32_e32 v190, 0x42800000, v207
	v_mul_f32_e32 v191, 0x42800000, v209
	v_cvt_pk_fp8_f32 v186, v190, v191 op_sel:[0,0,1]
	v_mul_f32_e32 v190, 0x42800000, v215
	v_mul_f32_e32 v191, 0x42800000, v217
	v_cvt_pk_fp8_f32 v187, v190, v191 op_sel:[0,0,1]
	v_lshl_add_u64 v[190:191], v[188:189], 0, v[142:143]
	global_store_dwordx4 v[190:191], v[180:183], off nt
	s_nop 1
	v_lshl_add_u64 v[180:181], v[188:189], 0, v[144:145]
	global_store_dwordx4 v[180:181], v[184:187], off nt
	s_waitcnt lgkmcnt(0)
	s_cbranch_execz .LBB0_291

; #define LAS __attribute__((address_space(3)))
; __device__ __forceinline__ unsigned stop_poll(const Ctx& c, const unsigned* p) {
;     volatile LAS unsigned* w = (volatile LAS unsigned*)(c.lds + STOPW_OFF);
;     if (c.wave == 0) { const unsigned v = __hip_atomic_load(p, __ATOMIC_RELAXED, __HIP_MEMORY_SCOPE_AGENT); if (c.lane == 0) *w = v; return (unsigned)__builtin_amdgcn_readfirstlane((int)v); }
;     return *w;
; __device__ __forceinline__ int conv_stream(const Ctx& c, int j, int first, int step, const unsigned* stop, const float* w_gu, const float* w_d, unsigned char* Wgu, unsigned char* Wd) {
;     ...
;         { const int i2 = i + step; const bool more = j + CONV_SLOTS * i2 < CONV_TOTAL && !(stop && stop_poll(c, stop) >= STOP_AT);
;           cs_load(j + CONV_SLOTS * (more ? i2 : i), c.lane, w_gu, w_d, va);
;           cs_store(c, j + CONV_SLOTS * i, vb, Wgu, Wd); i = i2; if (!more) break; }
.LBB0_274:
	s_cmp_gt_i32 s19, 0x17fff
	s_mov_b64 s[46:47], 0
	s_cbranch_scc1 .LBB0_282
	s_and_b64 vcc, exec, s[6:7]
	s_cbranch_vccz .LBB0_277
	s_nop 0
	v_mov_b32_e32 v2, s18
	ds_read_b32 v2, v2
	s_mov_b64 s[44:45], 0
	s_waitcnt lgkmcnt(0)
	v_readfirstlane_b32 s20, v2

; #define LAS __attribute__((address_space(3)))
; __device__ __forceinline__ void t128_load(const float* W, int N, int item, int lane, f32x4 (&v)[16]) {
;     const int nblk = N / 32, kb = item / nblk, nb = item % nblk, k0 = 128 * kb, n0 = 32 * nb;
; #pragma unroll
;     for (int i = 0; i < 16; ++i) v[i] = __builtin_nontemporal_load((const f32x4*)(W + (size_t)(k0 + i * 8 + (lane >> 3)) * N + n0 + (lane & 7) * 4));
; }
; template <int MODE>
; __device__ __forceinline__ void t128_store(const Ctx& c, const f32x4 (&v)[16], int K, int N, unsigned char* WT, int item) {
;     LAS float* scr = (LAS float*)(c.lds + c.wave * CONV_SCR);
;     const int nblk = N / 32, kb = item / nblk, nb = item % nblk, k0 = 128 * kb, n0 = 32 * nb, lane = c.lane;
; #pragma unroll
;     for (int i = 0; i < 16; ++i) { LAS float* d = scr + (i * 8 + (lane >> 3)) * 33 + (lane & 7) * 4; d[0] = v[i].x; d[1] = v[i].y; d[2] = v[i].z; d[3] = v[i].w; }
; __device__ __forceinline__ int conv_stream(const Ctx& c, int j, int first, int step, const unsigned* stop, const float* w_gu, const float* w_d, unsigned char* Wgu, unsigned char* Wd) {
;     ...
;         { const int i2 = i + step; const bool more = j + CONV_SLOTS * i2 < CONV_TOTAL && !(stop && stop_poll(c, stop) >= STOP_AT);
;           cs_load(j + CONV_SLOTS * (more ? i2 : i), c.lane, w_gu, w_d, va);
;           cs_store(c, j + CONV_SLOTS * i, vb, Wgu, Wd); i = i2; if (!more) break; }
.LBB0_286:
	s_nop 0
	v_or_b32_e32 v58, s21, v131
	v_ashrrev_i32_e32 v59, 31, v58
	v_lshlrev_b64 v[2:3], s46, v[58:59]
	v_add_u32_e32 v4, 8, v58
	v_add_u32_e32 v10, 16, v58
	v_add_u32_e32 v12, 24, v58
	v_add_u32_e32 v18, 32, v58
	v_add_u32_e32 v20, 40, v58
	v_add_u32_e32 v26, 48, v58
	v_add_u32_e32 v28, 56, v58
	v_add_u32_e32 v34, 64, v58
	v_add_u32_e32 v36, 0x48, v58
	v_add_u32_e32 v42, 0x50, v58
	v_add_u32_e32 v44, 0x58, v58
	v_add_u32_e32 v50, 0x60, v58
	v_add_u32_e32 v52, 0x68, v58
	v_add_u32_e32 v62, 0x70, v58
	v_add_u32_e32 v58, 0x78, v58
	v_ashrrev_i32_e32 v5, 31, v4
	v_ashrrev_i32_e32 v11, 31, v10
	v_ashrrev_i32_e32 v13, 31, v12
	v_ashrrev_i32_e32 v19, 31, v18
	v_ashrrev_i32_e32 v21, 31, v20
	v_ashrrev_i32_e32 v27, 31, v26
	v_ashrrev_i32_e32 v29, 31, v28
	v_ashrrev_i32_e32 v35, 31, v34
	v_ashrrev_i32_e32 v37, 31, v36
	v_ashrrev_i32_e32 v43, 31, v42
	v_ashrrev_i32_e32 v45, 31, v44
	v_ashrrev_i32_e32 v51, 31, v50
	v_ashrrev_i32_e32 v53, 31, v52
	v_ashrrev_i32_e32 v63, 31, v62
	v_ashrrev_i32_e32 v59, 31, v58
	v_lshl_add_u64 v[60:61], s[48:49], 0, v[132:133]
	v_lshlrev_b64 v[4:5], s46, v[4:5]
	v_lshlrev_b64 v[10:11], s46, v[10:11]
	v_lshlrev_b64 v[12:13], s46, v[12:13]
	v_lshlrev_b64 v[18:19], s46, v[18:19]
	v_lshlrev_b64 v[20:21], s46, v[20:21]
	v_lshlrev_b64 v[26:27], s46, v[26:27]
	v_lshlrev_b64 v[28:29], s46, v[28:29]
	v_lshlrev_b64 v[34:35], s46, v[34:35]
	v_lshlrev_b64 v[36:37], s46, v[36:37]
	v_lshlrev_b64 v[42:43], s46, v[42:43]
	v_lshlrev_b64 v[44:45], s46, v[44:45]
	v_lshlrev_b64 v[50:51], s46, v[50:51]
	v_lshlrev_b64 v[52:53], s46, v[52:53]
	v_lshlrev_b64 v[62:63], s46, v[62:63]
	v_lshlrev_b64 v[58:59], s46, v[58:59]
	v_lshl_add_u64 v[2:3], v[60:61], 0, v[2:3]
	v_lshl_add_u64 v[4:5], v[60:61], 0, v[4:5]
	v_lshl_add_u64 v[10:11], v[60:61], 0, v[10:11]
	v_lshl_add_u64 v[12:13], v[60:61], 0, v[12:13]
	v_lshl_add_u64 v[18:19], v[60:61], 0, v[18:19]
	v_lshl_add_u64 v[20:21], v[60:61], 0, v[20:21]
	v_lshl_add_u64 v[26:27], v[60:61], 0, v[26:27]
	v_lshl_add_u64 v[28:29], v[60:61], 0, v[28:29]
	v_lshl_add_u64 v[34:35], v[60:61], 0, v[34:35]
	v_lshl_add_u64 v[36:37], v[60:61], 0, v[36:37]
	v_lshl_add_u64 v[42:43], v[60:61], 0, v[42:43]
	v_lshl_add_u64 v[44:45], v[60:61], 0, v[44:45]
	v_lshl_add_u64 v[50:51], v[60:61], 0, v[50:51]
	v_lshl_add_u64 v[52:53], v[60:61], 0, v[52:53]
	v_lshl_add_u64 v[62:63], v[60:61], 0, v[62:63]
	v_lshl_add_u64 v[58:59], v[60:61], 0, v[58:59]
	s_and_b64 vcc, exec, s[44:45]
	s_cbranch_vccnz .LLcv1b_noload_w
	global_load_dwordx4 v[6:9], v[2:3], off nt
	s_nop 0
	global_load_dwordx4 v[2:5], v[4:5], off nt
	s_nop 0
	global_load_dwordx4 v[14:17], v[10:11], off nt
	s_nop 0
	global_load_dwordx4 v[10:13], v[12:13], off nt
	s_nop 0
	global_load_dwordx4 v[22:25], v[18:19], off nt
	s_nop 0
	global_load_dwordx4 v[18:21], v[20:21], off nt
	s_nop 0
	global_load_dwordx4 v[30:33], v[26:27], off nt
	s_nop 0
	global_load_dwordx4 v[26:29], v[28:29], off nt
	s_nop 0
	global_load_dwordx4 v[38:41], v[34:35], off nt
	s_nop 0
	global_load_dwordx4 v[34:37], v[36:37], off nt
	s_nop 0
	global_load_dwordx4 v[46:49], v[42:43], off nt
	s_nop 0
	global_load_dwordx4 v[42:45], v[44:45], off nt
	s_nop 0
	global_load_dwordx4 v[54:57], v[50:51], off nt
	s_nop 0
	global_load_dwordx4 v[50:53], v[52:53], off nt
	s_nop 0
	global_load_dwordx4 v[62:65], v[62:63], off nt
	s_nop 0
	global_load_dwordx4 v[58:61], v[58:59], off nt
	s_waitcnt vmcnt(20)
	s_branch .Lcv1b_noload
.LLcv1b_noload_w:
	s_waitcnt vmcnt(4)
.Lcv1b_noload:
	s_cmpk_gt_i32 s24, 0x7fff
	s_mov_b64 s[46:47], -1
	s_cbranch_scc0 .LBB0_288
	ds_write2_b32 v146, v70, v71 offset1:1
	ds_write2_b32 v146, v72, v73 offset0:2 offset1:3
	ds_write2_b32 v151, v66, v67 offset1:1
	ds_write2_b32 v151, v68, v69 offset0:2 offset1:3
	ds_write2_b32 v152, v78, v79 offset1:1
	ds_write2_b32 v152, v80, v81 offset0:2 offset1:3
	ds_write2_b32 v153, v74, v75 offset1:1
	ds_write2_b32 v153, v76, v77 offset0:2 offset1:3
	ds_write2_b32 v156, v86, v87 offset1:1
	ds_write2_b32 v157, v88, v89 offset1:1
	ds_write2_b32 v158, v82, v83 offset1:1
	ds_write2_b32 v159, v84, v85 offset1:1
	ds_write2_b32 v160, v94, v95 offset1:1
	ds_write2_b32 v161, v96, v97 offset1:1
	ds_write2_b32 v162, v90, v91 offset1:1
	ds_write2_b32 v163, v92, v93 offset1:1
	ds_write2_b32 v164, v102, v103 offset1:1
	ds_write2_b32 v165, v104, v105 offset1:1
	ds_write2_b32 v166, v98, v99 offset1:1
	ds_write2_b32 v167, v100, v101 offset1:1
	ds_write2_b32 v168, v110, v111 offset1:1
	ds_write2_b32 v169, v112, v113 offset1:1
	ds_write2_b32 v170, v106, v107 offset1:1
	ds_write2_b32 v171, v108, v109 offset1:1
	ds_write2_b32 v172, v118, v119 offset1:1
	ds_write2_b32 v173, v120, v121 offset1:1
	ds_write2_b32 v174, v114, v115 offset1:1
	ds_write2_b32 v175, v116, v117 offset1:1
	ds_write2_b32 v176, v126, v127 offset1:1
	ds_write2_b32 v177, v128, v129 offset1:1
	ds_write2_b32 v178, v122, v123 offset1:1
	ds_write2_b32 v179, v124, v125 offset1:1
	s_waitcnt lgkmcnt(0)
	ds_read2_b32 v[184:185], v150 offset1:8
	ds_read2_b32 v[186:187], v150 offset0:33 offset1:41
	ds_read2_b32 v[190:191], v150 offset0:66 offset1:74
	ds_read2_b32 v[192:193], v150 offset0:99 offset1:107
	v_mov_b32_e32 v180, v133
	ds_read2_b32 v[194:195], v150 offset0:132 offset1:140
	ds_read2_b32 v[196:197], v150 offset0:165 offset1:173
	s_waitcnt lgkmcnt(5)
	v_mul_f32_e32 v132, 0x42800000, v184
	s_waitcnt lgkmcnt(4)
	v_mul_f32_e32 v181, 0x42800000, v186
	v_cvt_pk_fp8_f32 v180, v132, v181
	s_waitcnt lgkmcnt(3)
	v_mul_f32_e32 v132, 0x42800000, v190
	s_waitcnt lgkmcnt(2)
	v_mul_f32_e32 v181, 0x42800000, v192
	ds_read2_b32 v[198:199], v150 offset0:198 offset1:206
	ds_read2_b32 v[200:201], v150 offset0:231 offset1:239
	v_cvt_pk_fp8_f32 v180, v132, v181 op_sel:[0,0,1]
	s_waitcnt lgkmcnt(3)
; #define LAS __attribute__((address_space(3)))
; template <int MODE>
; __device__ __forceinline__ void t128_store(const Ctx& c, const f32x4 (&v)[16], int K, int N, unsigned char* WT, int item) {
;     ...
;     const int cc = lane & 7;
; #pragma unroll
;     for (int j = 0; j < 4; ++j) { const int n = (lane >> 3) + 8 * j; const LAS float* s = scr + (16 * cc) * 33 + n; int w[4];
; #pragma unroll
;         for (int q = 0; q < 4; ++q) { int t = 0; t = __builtin_amdgcn_cvt_pk_fp8_f32(s[(4 * q) * 33] * WSCALE, s[(4 * q + 1) * 33] * WSCALE, t, false);
;             t = __builtin_amdgcn_cvt_pk_fp8_f32(s[(4 * q + 2) * 33] * WSCALE, s[(4 * q + 3) * 33] * WSCALE, t, true); w[q] = t; }
;         const int dr = drow_of<MODE>(n0 + n);
;         __builtin_nontemporal_store((u32x4){(unsigned)w[0], (unsigned)w[1], (unsigned)w[2], (unsigned)w[3]}, (u32x4*)(WT + (size_t)dr * K + k0 + 16 * cc)); }
	v_mul_f32_e32 v132, 0x42800000, v194
	s_waitcnt lgkmcnt(2)
	v_mul_f32_e32 v182, 0x42800000, v196
	v_mov_b32_e32 v181, v133
	ds_read2_b32 v[202:203], v155 offset0:8 offset1:16
	ds_read2_b32 v[204:205], v155 offset0:41 offset1:49
	v_cvt_pk_fp8_f32 v181, v132, v182
	ds_read2_b32 v[206:207], v155 offset0:74 offset1:82
	ds_read2_b32 v[208:209], v155 offset0:107 offset1:115
	ds_read2_b32 v[210:211], v155 offset0:140 offset1:148
	ds_read2_b32 v[212:213], v155 offset0:173 offset1:181
	s_waitcnt lgkmcnt(7)
	v_mul_f32_e32 v132, 0x42800000, v198
	s_waitcnt lgkmcnt(6)
	v_mul_f32_e32 v182, 0x42800000, v200
	v_cvt_pk_fp8_f32 v181, v132, v182 op_sel:[0,0,1]
	s_waitcnt lgkmcnt(5)
	v_mul_f32_e32 v132, 0x42800000, v202
	s_waitcnt lgkmcnt(4)
	v_mul_f32_e32 v183, 0x42800000, v204
	v_mov_b32_e32 v182, v133
	ds_read2_b32 v[214:215], v155 offset0:206 offset1:214
	ds_read2_b32 v[216:217], v155 offset0:239 offset1:247
	v_cvt_pk_fp8_f32 v182, v132, v183
	s_waitcnt lgkmcnt(3)
	v_mul_f32_e32 v186, 0x42800000, v210
	s_waitcnt lgkmcnt(2)
	v_mul_f32_e32 v190, 0x42800000, v212
	v_mov_b32_e32 v183, v133
	v_cvt_pk_fp8_f32 v183, v186, v190
	v_mul_f32_e32 v132, 0x42800000, v206
	v_mul_f32_e32 v184, 0x42800000, v208
	v_cvt_pk_fp8_f32 v182, v132, v184 op_sel:[0,0,1]
	s_waitcnt lgkmcnt(1)
	v_mul_f32_e32 v132, 0x42800000, v214
	s_waitcnt lgkmcnt(0)
	v_mul_f32_e32 v184, 0x42800000, v216
	v_cvt_pk_fp8_f32 v183, v132, v184 op_sel:[0,0,1]
	v_mul_f32_e32 v132, 0x42800000, v185
	v_mul_f32_e32 v185, 0x42800000, v187
	v_mov_b32_e32 v184, v133
	v_cvt_pk_fp8_f32 v184, v132, v185
	v_mul_f32_e32 v187, 0x42800000, v195
	v_mul_f32_e32 v190, 0x42800000, v197
	v_mov_b32_e32 v185, v133
	v_cvt_pk_fp8_f32 v185, v187, v190
	v_mul_f32_e32 v132, 0x42800000, v191
	v_mul_f32_e32 v186, 0x42800000, v193
	v_cvt_pk_fp8_f32 v184, v132, v186 op_sel:[0,0,1]
	v_mul_f32_e32 v132, 0x42800000, v199
	v_mul_f32_e32 v186, 0x42800000, v201
	s_add_i32 s20, s19, 0xffff7c00
	v_cvt_pk_fp8_f32 v185, v132, v186 op_sel:[0,0,1]
	v_mul_f32_e32 v132, 0x42800000, v203
	v_mul_f32_e32 v187, 0x42800000, v205
	v_mov_b32_e32 v186, v133
	s_lshr_b32 s42, s20, 11
	v_cvt_pk_fp8_f32 v186, v132, v187
	v_mul_f32_e32 v191, 0x42800000, v211
	v_mul_f32_e32 v192, 0x42800000, v213
	v_mov_b32_e32 v187, v133
	s_lshl_b64 s[20:21], s[42:43], 23
	v_cvt_pk_fp8_f32 v187, v191, v192
	s_add_u32 s20, s38, s20
	s_addc_u32 s21, s39, s21
	s_and_b32 s25, s24, 0x780
	v_mul_f32_e32 v132, 0x42800000, v207
	v_mul_f32_e32 v190, 0x42800000, v209
	s_add_u32 s20, s20, s25
	v_cvt_pk_fp8_f32 v186, v132, v190 op_sel:[0,0,1]
	v_mul_f32_e32 v132, 0x42800000, v215
	v_mul_f32_e32 v190, 0x42800000, v217
	s_addc_u32 s21, s21, 0
	v_cvt_pk_fp8_f32 v187, v132, v190 op_sel:[0,0,1]
	v_lshl_add_u64 v[188:189], s[20:21], 0, v[134:135]
	ds_read2_b32 v[190:191], v150 offset0:16 offset1:24
	ds_read2_b32 v[192:193], v150 offset0:49 offset1:57
	v_lshl_add_u64 v[218:219], v[188:189], 0, v[138:139]
	global_store_dwordx4 v[218:219], v[180:183], off nt
	s_mov_b64 s[46:47], 0
	s_waitcnt lgkmcnt(1)
	v_mul_f32_e32 v132, 0x42800000, v190
	v_lshl_add_u64 v[180:181], v[188:189], 0, v[140:141]
	global_store_dwordx4 v[180:181], v[184:187], off nt
	ds_read2_b32 v[184:185], v150 offset0:82 offset1:90
	ds_read2_b32 v[186:187], v150 offset0:115 offset1:123
	s_waitcnt lgkmcnt(2)
	v_mul_f32_e32 v181, 0x42800000, v192
	v_mov_b32_e32 v180, v133
	ds_read2_b32 v[194:195], v150 offset0:148 offset1:156
	ds_read2_b32 v[196:197], v150 offset0:181 offset1:189
	v_cvt_pk_fp8_f32 v180, v132, v181
	s_waitcnt lgkmcnt(3)
	v_mul_f32_e32 v132, 0x42800000, v184
	s_waitcnt lgkmcnt(2)
	v_mul_f32_e32 v181, 0x42800000, v186
	ds_read2_b32 v[198:199], v150 offset0:214 offset1:222
	ds_read2_b32 v[200:201], v150 offset0:247 offset1:255
	v_cvt_pk_fp8_f32 v180, v132, v181 op_sel:[0,0,1]
	s_waitcnt lgkmcnt(3)
	v_mul_f32_e32 v132, 0x42800000, v194
	s_waitcnt lgkmcnt(2)
	v_mul_f32_e32 v182, 0x42800000, v196
	v_mov_b32_e32 v181, v133
	ds_read2_b32 v[202:203], v155 offset0:24 offset1:32
	ds_read2_b32 v[204:205], v155 offset0:57 offset1:65
	v_cvt_pk_fp8_f32 v181, v132, v182
	ds_read2_b32 v[206:207], v155 offset0:90 offset1:98
	ds_read2_b32 v[208:209], v155 offset0:123 offset1:131
	ds_read2_b32 v[210:211], v155 offset0:156 offset1:164
	ds_read2_b32 v[212:213], v155 offset0:189 offset1:197
	s_waitcnt lgkmcnt(7)
	v_mul_f32_e32 v132, 0x42800000, v198
	s_waitcnt lgkmcnt(6)
	v_mul_f32_e32 v182, 0x42800000, v200
	v_cvt_pk_fp8_f32 v181, v132, v182 op_sel:[0,0,1]
	s_waitcnt lgkmcnt(5)
	v_mul_f32_e32 v132, 0x42800000, v202
	s_waitcnt lgkmcnt(4)
	v_mul_f32_e32 v183, 0x42800000, v204
	v_mov_b32_e32 v182, v133
	ds_read2_b32 v[214:215], v155 offset0:222 offset1:230
	ds_read2_b32 v[216:217], v154 offset0:127 offset1:135
	v_cvt_pk_fp8_f32 v182, v132, v183
	s_waitcnt lgkmcnt(3)
	v_mul_f32_e32 v186, 0x42800000, v210
	s_waitcnt lgkmcnt(2)
	v_mul_f32_e32 v190, 0x42800000, v212
	v_mov_b32_e32 v183, v133
	v_cvt_pk_fp8_f32 v183, v186, v190
	v_mul_f32_e32 v132, 0x42800000, v206
	v_mul_f32_e32 v184, 0x42800000, v208
	v_cvt_pk_fp8_f32 v182, v132, v184 op_sel:[0,0,1]
	s_waitcnt lgkmcnt(1)
	v_mul_f32_e32 v132, 0x42800000, v214
	s_waitcnt lgkmcnt(0)
	v_mul_f32_e32 v184, 0x42800000, v216
	v_cvt_pk_fp8_f32 v183, v132, v184 op_sel:[0,0,1]
	v_mul_f32_e32 v132, 0x42800000, v191
	v_mul_f32_e32 v186, 0x42800000, v193
	v_mov_b32_e32 v184, v133
	v_cvt_pk_fp8_f32 v184, v132, v186
	v_mul_f32_e32 v132, 0x42800000, v185
	v_mul_f32_e32 v186, 0x42800000, v187
	v_mul_f32_e32 v187, 0x42800000, v195
	v_mul_f32_e32 v190, 0x42800000, v197
	v_mov_b32_e32 v185, v133
	v_cvt_pk_fp8_f32 v185, v187, v190
	v_cvt_pk_fp8_f32 v184, v132, v186 op_sel:[0,0,1]
	v_mul_f32_e32 v132, 0x42800000, v199
	v_mul_f32_e32 v186, 0x42800000, v201
	v_cvt_pk_fp8_f32 v185, v132, v186 op_sel:[0,0,1]
	v_mul_f32_e32 v132, 0x42800000, v203
	v_mul_f32_e32 v187, 0x42800000, v205
	v_mov_b32_e32 v186, v133
	v_cvt_pk_fp8_f32 v186, v132, v187
	v_mul_f32_e32 v191, 0x42800000, v211
	v_mul_f32_e32 v192, 0x42800000, v213
	v_mov_b32_e32 v187, v133
	v_cvt_pk_fp8_f32 v187, v191, v192
	v_mul_f32_e32 v132, 0x42800000, v207
	v_mul_f32_e32 v190, 0x42800000, v209
	v_cvt_pk_fp8_f32 v186, v132, v190 op_sel:[0,0,1]
	v_mul_f32_e32 v132, 0x42800000, v215
	v_mul_f32_e32 v190, 0x42800000, v217
	v_cvt_pk_fp8_f32 v187, v132, v190 op_sel:[0,0,1]
	v_lshl_add_u64 v[190:191], v[188:189], 0, v[142:143]
	global_store_dwordx4 v[190:191], v[180:183], off nt
	s_nop 1
	v_lshl_add_u64 v[180:181], v[188:189], 0, v[144:145]
	global_store_dwordx4 v[180:181], v[184:187], off nt
	s_waitcnt lgkmcnt(0)

; #define LAS __attribute__((address_space(3)))
; __device__ __forceinline__ unsigned stop_poll(const Ctx& c, const unsigned* p) {
;     volatile LAS unsigned* w = (volatile LAS unsigned*)(c.lds + STOPW_OFF);
;     if (c.wave == 0) { const unsigned v = __hip_atomic_load(p, __ATOMIC_RELAXED, __HIP_MEMORY_SCOPE_AGENT); if (c.lane == 0) *w = v; return (unsigned)__builtin_amdgcn_readfirstlane((int)v); }
;     return *w;
; __device__ __forceinline__ int conv_stream(const Ctx& c, int j, int first, int step, const unsigned* stop, const float* w_gu, const float* w_d, unsigned char* Wgu, unsigned char* Wd) {
;     ...
;         { const int i2 = i + step; const bool more = j + CONV_SLOTS * i2 < CONV_TOTAL && !(stop && stop_poll(c, stop) >= STOP_AT);
;           cs_load(j + CONV_SLOTS * (more ? i2 : i), c.lane, w_gu, w_d, vb);
.LBB0_660:
	s_add_i32 s26, s25, 0xfffffc00
	s_cmp_gt_i32 s26, 0x17fff
	s_mov_b64 s[56:57], 0
	s_cbranch_scc1 .LBB0_668
	s_mov_b64 s[56:57], -1
	s_and_b64 vcc, exec, s[52:53]
	s_cbranch_vccz .LBB0_663
	s_waitcnt vmcnt(20)
	v_mov_b32_e32 v66, s24
	ds_read_b32 v66, v66
	s_mov_b64 s[56:57], 0
	s_waitcnt lgkmcnt(0)
	v_readfirstlane_b32 s20, v66

; __device__ __forceinline__ void t128_load(const float* W, int N, int item, int lane, f32x4 (&v)[16]) {
;     const int nblk = N / 32, kb = item / nblk, nb = item % nblk, k0 = 128 * kb, n0 = 32 * nb;
; #pragma unroll
;     for (int i = 0; i < 16; ++i) v[i] = __builtin_nontemporal_load((const f32x4*)(W + (size_t)(k0 + i * 8 + (lane >> 3)) * N + n0 + (lane & 7) * 4));
; __device__ __forceinline__ int conv_stream(const Ctx& c, int j, int first, int step, const unsigned* stop, const float* w_gu, const float* w_d, unsigned char* Wgu, unsigned char* Wd) {
;     ...
;         { const int i2 = i + step; const bool more = j + CONV_SLOTS * i2 < CONV_TOTAL && !(stop && stop_poll(c, stop) >= STOP_AT);
;           cs_load(j + CONV_SLOTS * (more ? i2 : i), c.lane, w_gu, w_d, vb);
;           cs_store(c, j + CONV_SLOTS * i, va, Wgu, Wd); i = i2; if (!more) break; }
.LBB0_672:
	s_nop 0
	v_or_b32_e32 v122, s21, v131
	v_ashrrev_i32_e32 v123, 31, v122
	v_lshlrev_b64 v[66:67], s58, v[122:123]
	v_add_u32_e32 v68, 8, v122
	v_add_u32_e32 v74, 16, v122
	v_add_u32_e32 v76, 24, v122
	v_add_u32_e32 v82, 32, v122
	v_add_u32_e32 v84, 40, v122
	v_add_u32_e32 v90, 48, v122
	v_add_u32_e32 v92, 56, v122
	v_add_u32_e32 v98, 64, v122
	v_add_u32_e32 v100, 0x48, v122
	v_add_u32_e32 v106, 0x50, v122
	v_add_u32_e32 v108, 0x58, v122
	v_add_u32_e32 v114, 0x60, v122
	v_add_u32_e32 v116, 0x68, v122
	v_add_u32_e32 v126, 0x70, v122
	v_add_u32_e32 v122, 0x78, v122
	v_lshlrev_b32_e32 v132, 2, v130
	v_ashrrev_i32_e32 v69, 31, v68
	v_ashrrev_i32_e32 v75, 31, v74
	v_ashrrev_i32_e32 v77, 31, v76
	v_ashrrev_i32_e32 v83, 31, v82
	v_ashrrev_i32_e32 v85, 31, v84
	v_ashrrev_i32_e32 v91, 31, v90
	v_ashrrev_i32_e32 v93, 31, v92
	v_ashrrev_i32_e32 v99, 31, v98
	v_ashrrev_i32_e32 v101, 31, v100
	v_ashrrev_i32_e32 v107, 31, v106
	v_ashrrev_i32_e32 v109, 31, v108
	v_ashrrev_i32_e32 v115, 31, v114
	v_ashrrev_i32_e32 v117, 31, v116
	v_ashrrev_i32_e32 v127, 31, v126
	v_ashrrev_i32_e32 v123, 31, v122
	v_lshl_add_u64 v[124:125], s[60:61], 0, v[132:133]
	v_lshlrev_b64 v[68:69], s58, v[68:69]
	v_lshlrev_b64 v[74:75], s58, v[74:75]
	v_lshlrev_b64 v[76:77], s58, v[76:77]
	v_lshlrev_b64 v[82:83], s58, v[82:83]
	v_lshlrev_b64 v[84:85], s58, v[84:85]
	v_lshlrev_b64 v[90:91], s58, v[90:91]
	v_lshlrev_b64 v[92:93], s58, v[92:93]
	v_lshlrev_b64 v[98:99], s58, v[98:99]
	v_lshlrev_b64 v[100:101], s58, v[100:101]
	v_lshlrev_b64 v[106:107], s58, v[106:107]
	v_lshlrev_b64 v[108:109], s58, v[108:109]
	v_lshlrev_b64 v[114:115], s58, v[114:115]
	v_lshlrev_b64 v[116:117], s58, v[116:117]
	v_lshlrev_b64 v[126:127], s58, v[126:127]
	v_lshlrev_b64 v[122:123], s58, v[122:123]
	v_lshl_add_u64 v[66:67], v[124:125], 0, v[66:67]
	v_lshl_add_u64 v[68:69], v[124:125], 0, v[68:69]
	v_lshl_add_u64 v[74:75], v[124:125], 0, v[74:75]
	v_lshl_add_u64 v[76:77], v[124:125], 0, v[76:77]
	v_lshl_add_u64 v[82:83], v[124:125], 0, v[82:83]
	v_lshl_add_u64 v[84:85], v[124:125], 0, v[84:85]
	v_lshl_add_u64 v[90:91], v[124:125], 0, v[90:91]
	v_lshl_add_u64 v[92:93], v[124:125], 0, v[92:93]
	v_lshl_add_u64 v[98:99], v[124:125], 0, v[98:99]
	v_lshl_add_u64 v[100:101], v[124:125], 0, v[100:101]
	v_lshl_add_u64 v[106:107], v[124:125], 0, v[106:107]
	v_lshl_add_u64 v[108:109], v[124:125], 0, v[108:109]
	v_lshl_add_u64 v[114:115], v[124:125], 0, v[114:115]
	v_lshl_add_u64 v[116:117], v[124:125], 0, v[116:117]
	v_lshl_add_u64 v[126:127], v[124:125], 0, v[126:127]
	v_lshl_add_u64 v[122:123], v[124:125], 0, v[122:123]
	s_and_b64 vcc, exec, s[56:57]
	s_cbranch_vccnz .Lcv3a_load
	s_waitcnt vmcnt(0)
	s_branch .Lcv3a_noload

; __device__ __forceinline__ void t128_load(const float* W, int N, int item, int lane, f32x4 (&v)[16]) {
;     const int nblk = N / 32, kb = item / nblk, nb = item % nblk, k0 = 128 * kb, n0 = 32 * nb;
; #pragma unroll
;     for (int i = 0; i < 16; ++i) v[i] = __builtin_nontemporal_load((const f32x4*)(W + (size_t)(k0 + i * 8 + (lane >> 3)) * N + n0 + (lane & 7) * 4));
; __device__ __forceinline__ int conv_stream(const Ctx& c, int j, int first, int step, const unsigned* stop, const float* w_gu, const float* w_d, unsigned char* Wgu, unsigned char* Wd) {
;     ...
;         { const int i2 = i + step; const bool more = j + CONV_SLOTS * i2 < CONV_TOTAL && !(stop && stop_poll(c, stop) >= STOP_AT);
;           cs_load(j + CONV_SLOTS * (more ? i2 : i), c.lane, w_gu, w_d, va);
;           cs_store(c, j + CONV_SLOTS * i, vb, Wgu, Wd); i = i2; if (!more) break; }
.LBB0_687:
	s_waitcnt vmcnt(20)
	v_or_b32_e32 v58, s21, v131
	v_ashrrev_i32_e32 v59, 31, v58
	v_lshlrev_b64 v[2:3], s58, v[58:59]
	v_add_u32_e32 v4, 8, v58
	v_add_u32_e32 v10, 16, v58
	v_add_u32_e32 v12, 24, v58
	v_add_u32_e32 v18, 32, v58
	v_add_u32_e32 v20, 40, v58
	v_add_u32_e32 v26, 48, v58
	v_add_u32_e32 v28, 56, v58
	v_add_u32_e32 v34, 64, v58
	v_add_u32_e32 v36, 0x48, v58
	v_add_u32_e32 v42, 0x50, v58
	v_add_u32_e32 v44, 0x58, v58
	v_add_u32_e32 v50, 0x60, v58
	v_add_u32_e32 v52, 0x68, v58
	v_add_u32_e32 v62, 0x70, v58
	v_add_u32_e32 v58, 0x78, v58
	v_ashrrev_i32_e32 v5, 31, v4
	v_ashrrev_i32_e32 v11, 31, v10
	v_ashrrev_i32_e32 v13, 31, v12
	v_ashrrev_i32_e32 v19, 31, v18
	v_ashrrev_i32_e32 v21, 31, v20
	v_ashrrev_i32_e32 v27, 31, v26
	v_ashrrev_i32_e32 v29, 31, v28
	v_ashrrev_i32_e32 v35, 31, v34
	v_ashrrev_i32_e32 v37, 31, v36
	v_ashrrev_i32_e32 v43, 31, v42
	v_ashrrev_i32_e32 v45, 31, v44
	v_ashrrev_i32_e32 v51, 31, v50
	v_ashrrev_i32_e32 v53, 31, v52
	v_ashrrev_i32_e32 v63, 31, v62
	v_ashrrev_i32_e32 v59, 31, v58
	v_lshl_add_u64 v[60:61], s[60:61], 0, v[132:133]
	v_lshlrev_b64 v[4:5], s58, v[4:5]
	v_lshlrev_b64 v[10:11], s58, v[10:11]
	v_lshlrev_b64 v[12:13], s58, v[12:13]
	v_lshlrev_b64 v[18:19], s58, v[18:19]
	v_lshlrev_b64 v[20:21], s58, v[20:21]
	v_lshlrev_b64 v[26:27], s58, v[26:27]
	v_lshlrev_b64 v[28:29], s58, v[28:29]
	v_lshlrev_b64 v[34:35], s58, v[34:35]
	v_lshlrev_b64 v[36:37], s58, v[36:37]
	v_lshlrev_b64 v[42:43], s58, v[42:43]
	v_lshlrev_b64 v[44:45], s58, v[44:45]
	v_lshlrev_b64 v[50:51], s58, v[50:51]
	v_lshlrev_b64 v[52:53], s58, v[52:53]
	v_lshlrev_b64 v[62:63], s58, v[62:63]
	v_lshlrev_b64 v[58:59], s58, v[58:59]
	v_lshl_add_u64 v[2:3], v[60:61], 0, v[2:3]
	v_lshl_add_u64 v[4:5], v[60:61], 0, v[4:5]
	v_lshl_add_u64 v[10:11], v[60:61], 0, v[10:11]
	v_lshl_add_u64 v[12:13], v[60:61], 0, v[12:13]
	v_lshl_add_u64 v[18:19], v[60:61], 0, v[18:19]
	v_lshl_add_u64 v[20:21], v[60:61], 0, v[20:21]
	v_lshl_add_u64 v[26:27], v[60:61], 0, v[26:27]
	v_lshl_add_u64 v[28:29], v[60:61], 0, v[28:29]
	v_lshl_add_u64 v[34:35], v[60:61], 0, v[34:35]
	v_lshl_add_u64 v[36:37], v[60:61], 0, v[36:37]
	v_lshl_add_u64 v[42:43], v[60:61], 0, v[42:43]
	v_lshl_add_u64 v[44:45], v[60:61], 0, v[44:45]
	v_lshl_add_u64 v[50:51], v[60:61], 0, v[50:51]
	v_lshl_add_u64 v[52:53], v[60:61], 0, v[52:53]
	v_lshl_add_u64 v[62:63], v[60:61], 0, v[62:63]
	v_lshl_add_u64 v[58:59], v[60:61], 0, v[58:59]
	s_and_b64 vcc, exec, s[56:57]
	s_cbranch_vccz .Lcv3b_load
	s_waitcnt vmcnt(0)
	s_branch .Lcv3b_noload

; __device__ __forceinline__ void drain_balanced(const Ctx& c, const unsigned* ctl, const float* w_gu, const float* w_d, unsigned char* Wgu, unsigned char* Wd) {
;     ...
;         auto item_of = [&](int v) -> int { while (v >= pre[s + 1]) ++s; return s + CONV_SLOTS * (prog[s] + (v - pre[s])); };
;         int v = lo; int it = __builtin_amdgcn_readfirstlane(item_of(v));
;         f32x4 va[16], vb[16];
;         cs_load(it, c.lane, w_gu, w_d, va);
;         for (;;) {
;             { const int v2 = v + 1; const bool more = v2 < hi; const int it2 = more ? __builtin_amdgcn_readfirstlane(item_of(v2)) : it;
.LBB0_1193:
	s_add_i32 s8, s40, 1
	s_cmp_lt_i32 s8, s18
	s_cselect_b64 s[12:13], -1, 0
	s_cmp_ge_i32 s8, s18
	s_cbranch_scc1 .LBB0_1198
	s_lshl_b32 s10, s19, 2
	s_add_i32 s10, s10, 0
	s_add_i32 s11, s10, 0x21004
	s_waitcnt vmcnt(20)
	v_mov_b32_e32 v66, s11
	ds_read_b32 v66, v66
	s_waitcnt lgkmcnt(0)
	v_cmp_lt_i32_e32 vcc, s8, v66
	s_cbranch_vccnz .LBB0_1197
	s_add_i32 s10, s10, 0x21008

; __device__ __forceinline__ void t128_load(const float* W, int N, int item, int lane, f32x4 (&v)[16]) {
;     const int nblk = N / 32, kb = item / nblk, nb = item % nblk, k0 = 128 * kb, n0 = 32 * nb;
; #pragma unroll
;     for (int i = 0; i < 16; ++i) v[i] = __builtin_nontemporal_load((const f32x4*)(W + (size_t)(k0 + i * 8 + (lane >> 3)) * N + n0 + (lane & 7) * 4));
; __device__ __forceinline__ void drain_balanced(const Ctx& c, const unsigned* ctl, const float* w_gu, const float* w_d, unsigned char* Wgu, unsigned char* Wd) {
;     ...
;             { const int v2 = v + 1; const bool more = v2 < hi; const int it2 = more ? __builtin_amdgcn_readfirstlane(item_of(v2)) : it;
;               cs_load(it2, c.lane, w_gu, w_d, vb); cs_store(c, it, va, Wgu, Wd); v = v2; it = it2; if (!more) break; }
.LBB0_1203:
	s_nop 0
	v_or_b32_e32 v122, s8, v131
	v_lshlrev_b32_e32 v132, 2, v130
	v_ashrrev_i32_e32 v123, 31, v122
	v_lshl_add_u64 v[124:125], s[16:17], 0, v[132:133]
	v_lshlrev_b64 v[66:67], s14, v[122:123]
	v_lshl_add_u64 v[74:75], v[124:125], 0, v[66:67]
	v_add_u32_e32 v66, 8, v122
	v_ashrrev_i32_e32 v67, 31, v66
	v_lshlrev_b64 v[66:67], s14, v[66:67]
	v_lshl_add_u64 v[76:77], v[124:125], 0, v[66:67]
	s_and_b64 vcc, exec, s[12:13]
	s_cbranch_vccnz .Lcv7a_load
	s_waitcnt vmcnt(0)
	s_branch .Lcv7a_noload

; __device__ __forceinline__ void t128_load(const float* W, int N, int item, int lane, f32x4 (&v)[16]) {
;     const int nblk = N / 32, kb = item / nblk, nb = item % nblk, k0 = 128 * kb, n0 = 32 * nb;
; #pragma unroll
;     for (int i = 0; i < 16; ++i) v[i] = __builtin_nontemporal_load((const f32x4*)(W + (size_t)(k0 + i * 8 + (lane >> 3)) * N + n0 + (lane & 7) * 4));
; __device__ __forceinline__ void drain_balanced(const Ctx& c, const unsigned* ctl, const float* w_gu, const float* w_d, unsigned char* Wgu, unsigned char* Wd) {
;     ...
;             { const int v2 = v + 1; const bool more = v2 < hi; const int it2 = more ? __builtin_amdgcn_readfirstlane(item_of(v2)) : it;
;               cs_load(it2, c.lane, w_gu, w_d, va); cs_store(c, it, vb, Wgu, Wd); v = v2; it = it2; if (!more) break; }
.LBB0_1217:
	s_waitcnt vmcnt(20)
	v_or_b32_e32 v58, s8, v131
	v_ashrrev_i32_e32 v59, 31, v58
	v_lshl_add_u64 v[60:61], s[16:17], 0, v[132:133]
	v_lshlrev_b64 v[2:3], s14, v[58:59]
	v_lshl_add_u64 v[10:11], v[60:61], 0, v[2:3]
	v_add_u32_e32 v2, 8, v58
	v_ashrrev_i32_e32 v3, 31, v2
	v_lshlrev_b64 v[2:3], s14, v[2:3]
	v_lshl_add_u64 v[12:13], v[60:61], 0, v[2:3]
	s_and_b64 vcc, exec, s[12:13]
	s_cbranch_vccz .Lcv7b_load
	s_waitcnt vmcnt(0)
	s_branch .Lcv7b_noload

; __device__ __forceinline__ void drain_balanced(const Ctx& c, const unsigned* ctl, const float* w_gu, const float* w_d, unsigned char* Wgu, unsigned char* Wd) {
;     ...
;         auto item_of = [&](int v) -> int { while (v >= pre[s + 1]) ++s; return s + CONV_SLOTS * (prog[s] + (v - pre[s])); };
;         int v = lo; int it = __builtin_amdgcn_readfirstlane(item_of(v));
;         f32x4 va[16], vb[16];
;         cs_load(it, c.lane, w_gu, w_d, va);
;         for (;;) {
;             { const int v2 = v + 1; const bool more = v2 < hi; const int it2 = more ? __builtin_amdgcn_readfirstlane(item_of(v2)) : it;
;               cs_load(it2, c.lane, w_gu, w_d, vb); cs_store(c, it, va, Wgu, Wd); v = v2; it = it2; if (!more) break; }
;             { const int v2 = v + 1; const bool more = v2 < hi; const int it2 = more ? __builtin_amdgcn_readfirstlane(item_of(v2)) : it;
.LBB0_1334:
	s_add_i32 s8, s34, 1
	s_cmp_lt_i32 s8, s18
	s_cselect_b64 s[12:13], -1, 0
	s_cmp_ge_i32 s8, s18
	s_cbranch_scc1 .LBB0_1339
	s_lshl_b32 s10, s19, 2
	s_add_i32 s10, s10, 0
	s_add_i32 s11, s10, 0x21004
	s_waitcnt vmcnt(20)
	v_mov_b32_e32 v66, s11
	ds_read_b32 v66, v66
	s_waitcnt lgkmcnt(0)
	v_cmp_lt_i32_e32 vcc, s8, v66
	s_cbranch_vccnz .LBB0_1338
	s_add_i32 s10, s10, 0x21008
